# baseline (speedup 1.0000x reference)
.LBB1_8:
	v_lshrrev_b32_e32 v7, 5, v2
	v_lshlrev_b32_e64 v9, v2, -2
	v_cmp_eq_u32_e64 s[44:45], v3, v7
	v_cmp_gt_u32_e32 vcc, v3, v7
	v_and_b32_e32 v9, v9, v6
	v_cndmask_b32_e64 v9, 0, v9, s[44:45]
	v_cndmask_b32_e32 v9, v9, v6, vcc
	v_cmp_ne_u32_e32 vcc, 0, v9
	s_and_b32 s19, vcc_lo, 0xffff
	s_cbranch_scc0 .LBB1_13
	s_ff1_i32_b32 s3, s19
	v_readlane_b32 s15, v9, s3
	s_ff1_i32_b32 s18, s15
	s_lshl_b32 s20, s3, 11
	s_lshl_b32 s21, s18, 6
	s_add_i32 s20, s20, s21
	v_lshl_or_b32 v7, v3, 2, s20
	ds_read_b32 v7, v7
	s_add_i32 s21, s15, -1
	s_and_b32 s15, s15, s21
	s_cbranch_scc1 .Lk2_same
	s_add_i32 s21, s19, -1
	s_and_b32 s19, s19, s21
	s_cbranch_scc0 .Lk2_single
	s_ff1_i32_b32 s3, s19
	v_readlane_b32 s15, v9, s3
.Lk2_same:
	s_ff1_i32_b32 s15, s15
	s_lshl_b32 s20, s3, 5
	s_or_b32 s22, s15, s20
	v_lshl_or_b32 v9, s22, 6, v4
	ds_read_b32 v9, v9
	s_waitcnt lgkmcnt(1)
	v_readlane_b32 s3, v7, s3
	s_lshr_b32 s3, s3, s15
	s_bitcmp0_b32 s3, 0
	s_cselect_b64 vcc, -1, 0
	s_waitcnt lgkmcnt(0)
	v_not_b32_e32 v9, v9
	v_cndmask_b32_e32 v9, -1, v9, vcc
	v_bitop3_b32 v6, v9, v6, v7 bitop3:0x40
	v_mov_b32_e32 v2, s22
	s_branch .LBB1_8
